# phase 3 kv/k_b norm loop: k_b loads hoisted to the iteration top and two tokens per trip (16 loads per lane in flight); plus phase 10 / phase 0 / router edits
# speedup vs baseline: 1.0093x; 1.0004x over previous
.LBB0_553:
	v_lshl_or_b32 v2, s2, 3, v1
	s_movk_i32 s3, 0x2000
	v_cmp_gt_i32_e32 vcc, s3, v2
	s_and_saveexec_b64 s[6:7], vcc
	v_readlane_b32 s82, v255, 2
	s_cbranch_execz .LBB0_556
	v_mbcnt_lo_u32_b32 v0, -1, 0
	v_mbcnt_hi_u32_b32 v3, -1, v0
	v_and_b32_e32 v0, 64, v3
	v_add_u32_e32 v4, 64, v0
	v_xor_b32_e32 v0, 32, v3
	v_cmp_lt_i32_e32 vcc, v0, v4
	v_xor_b32_e32 v5, 16, v3
	s_load_dwordx2 s[4:5], s[0:1], 0x58
	s_load_dwordx2 s[10:11], s[0:1], 0x68
	v_cndmask_b32_e32 v0, v3, v0, vcc
	v_cmp_lt_i32_e32 vcc, v5, v4
	s_waitcnt vmcnt(0)
	v_lshlrev_b32_e32 v6, 4, v217
	v_mov_b32_e32 v7, 0
	v_cndmask_b32_e32 v5, v3, v5, vcc
	v_lshlrev_b32_e32 v12, 2, v5
	v_xor_b32_e32 v5, 8, v3
	v_cmp_lt_i32_e32 vcc, v5, v4
	s_waitcnt lgkmcnt(0)
	s_lshl_b32 s8, s80, 3
	s_ashr_i32 s9, s8, 31
	v_cndmask_b32_e32 v5, v3, v5, vcc
	v_lshlrev_b32_e32 v13, 2, v5
	v_xor_b32_e32 v5, 4, v3
	v_cmp_lt_i32_e32 vcc, v5, v4
	v_lshlrev_b32_e32 v0, 2, v0
	s_lshl_b64 s[12:13], s[8:9], 9
	v_cndmask_b32_e32 v5, v3, v5, vcc
	v_lshlrev_b32_e32 v14, 2, v5
	v_xor_b32_e32 v5, 2, v3
	v_cmp_lt_i32_e32 vcc, v5, v4
	s_mov_b64 s[14:15], 0
	s_mov_b32 s3, 0x800000
	v_cndmask_b32_e32 v5, v3, v5, vcc
	v_lshlrev_b32_e32 v15, 2, v5
	v_xor_b32_e32 v5, 1, v3
	v_cmp_lt_i32_e32 vcc, v5, v4
	s_mov_b64 s[16:17], 0x21b38000
	s_mov_b32 s18, 0x21b38000
	v_cndmask_b32_e32 v3, v3, v5, vcc
	v_lshlrev_b32_e32 v16, 2, v3
	v_lshlrev_b32_e32 v3, 6, v250
	v_lshl_add_u64 v[4:5], s[4:5], 0, v[6:7]
	v_and_b32_e32 v6, 0x1c0, v3
	v_ashrrev_i32_e32 v3, 31, v2
	v_lshlrev_b64 v[8:9], 11, v[2:3]
	v_lshlrev_b64 v[10:11], 9, v[2:3]
	v_lshl_add_u64 v[6:7], s[10:11], 0, v[6:7]
	v_lshl_or_b32 v8, v217, 5, v8
	s_lshl_b64 s[10:11], s[8:9], 11
	v_lshl_or_b32 v10, v217, 3, v10
	v_mov_b32_e32 v3, 0x358637bd
	s_mov_b32 s9, 0x1ef38000
	s_movk_i32 s19, 0x1fff
	s_cmp_eq_u32 s80, 0x100
	s_cbranch_scc0 .LBB0_555
.Lp3_fast:
	v_lshl_add_u64 v[22:23], s[76:77], 0, v[10:11]
	v_add_co_u32_e32 v26, vcc, 0x1e738000, v22
	global_load_dwordx4 v[18:21], v[4:5], off
	s_nop 0
	v_addc_co_u32_e32 v27, vcc, 0, v23, vcc
	global_load_dwordx2 v[26:27], v[26:27], off
	v_add_co_u32_e64 v22, s[4:5], s9, v22
	v_lshl_add_u64 v[24:25], s[76:77], 0, v[8:9]
	s_nop 0
	v_addc_co_u32_e64 v23, vcc, 0, v23, s[4:5]
	v_add_co_u32_e32 v44, vcc, s18, v24
	v_lshl_add_u64 v[42:43], v[24:25], 0, s[16:17]
	s_nop 0
	v_addc_co_u32_e32 v45, vcc, 0, v25, vcc
	v_add_u32_e32 v2, s8, v2
	v_cmp_lt_i32_e32 vcc, s19, v2
	s_or_b64 s[14:15], vcc, s[14:15]
	v_lshl_add_u64 v[8:9], v[8:9], 0, s[10:11]
	v_lshl_add_u64 v[10:11], v[10:11], 0, s[12:13]
	global_load_dwordx4 v[60:63], v[44:45], off
	global_load_dwordx4 v[64:67], v[42:43], off offset:16
	global_load_dwordx4 v[68:71], v[6:7], off
	global_load_dwordx4 v[72:75], v[6:7], off offset:16
	global_load_dwordx4 v[76:79], v[6:7], off offset:32
	global_load_dwordx4 v[80:83], v[6:7], off offset:48
	v_lshl_add_u64 v[92:93], s[76:77], 0, v[10:11]
	v_add_co_u32_e32 v96, vcc, 0x1e738000, v92
	global_load_dwordx4 v[88:91], v[4:5], off
	s_nop 0
	v_addc_co_u32_e32 v97, vcc, 0, v93, vcc
	global_load_dwordx2 v[96:97], v[96:97], off
	v_add_co_u32_e64 v92, s[4:5], s9, v92
	v_lshl_add_u64 v[94:95], s[76:77], 0, v[8:9]
	s_nop 0
	v_addc_co_u32_e64 v93, vcc, 0, v93, s[4:5]
	v_add_co_u32_e32 v114, vcc, s18, v94
	v_lshl_add_u64 v[112:113], v[94:95], 0, s[16:17]
	s_nop 0
	v_addc_co_u32_e32 v115, vcc, 0, v95, vcc
	v_add_u32_e32 v2, s8, v2
	v_cmp_lt_i32_e32 vcc, s19, v2
	s_or_b64 s[14:15], vcc, s[14:15]
	v_lshl_add_u64 v[8:9], v[8:9], 0, s[10:11]
	v_lshl_add_u64 v[10:11], v[10:11], 0, s[12:13]
	global_load_dwordx4 v[160:163], v[114:115], off
	global_load_dwordx4 v[164:167], v[112:113], off offset:16
	global_load_dwordx4 v[168:171], v[6:7], off
	global_load_dwordx4 v[172:175], v[6:7], off offset:16
	global_load_dwordx4 v[176:179], v[6:7], off offset:32
	global_load_dwordx4 v[180:183], v[6:7], off offset:48
	s_waitcnt vmcnt(14)
	v_lshlrev_b32_e32 v24, 16, v26
	v_and_b32_e32 v25, 0xffff0000, v26
	v_and_b32_e32 v26, 0xffff0000, v27
	v_lshlrev_b32_e32 v27, 16, v27
	v_pk_mul_f32 v[28:29], v[24:25], v[24:25]
	v_pk_mul_f32 v[30:31], v[26:27], v[26:27]
	v_add_f32_e32 v17, v28, v29
	v_add_f32_e32 v17, v31, v17
	v_add_f32_e32 v17, v30, v17
	ds_bpermute_b32 v28, v0, v17
	s_waitcnt lgkmcnt(0)
	v_add_f32_e32 v17, v17, v28
	ds_bpermute_b32 v28, v12, v17
	s_waitcnt lgkmcnt(0)
	v_add_f32_e32 v17, v17, v28
	ds_bpermute_b32 v28, v13, v17
	s_waitcnt lgkmcnt(0)
	v_add_f32_e32 v17, v17, v28
	ds_bpermute_b32 v28, v14, v17
	s_waitcnt lgkmcnt(0)
	v_add_f32_e32 v17, v17, v28
	ds_bpermute_b32 v28, v15, v17
	s_waitcnt lgkmcnt(0)
	v_add_f32_e32 v17, v17, v28
	ds_bpermute_b32 v28, v16, v17
	s_waitcnt lgkmcnt(0)
	v_add_f32_e32 v17, v17, v28
	v_fmamk_f32 v17, v17, 0x3b800000, v3
	v_mul_f32_e32 v28, 0x4b800000, v17
	v_cmp_gt_f32_e32 vcc, s3, v17
	s_nop 1
	v_cndmask_b32_e32 v17, v17, v28, vcc
	v_rsq_f32_e32 v17, v17
	s_nop 0
	v_mul_f32_e32 v28, 0x45800000, v17
	v_cndmask_b32_e32 v17, v17, v28, vcc
	v_mul_f32_e32 v24, v17, v24
	v_mul_f32_e32 v25, v17, v25
	v_mul_f32_e32 v27, v17, v27
	v_mul_f32_e32 v17, v17, v26
	v_mul_f32_e32 v18, v18, v24
	v_mul_f32_e32 v19, v19, v25
	v_mul_f32_e32 v20, v20, v27
	v_mul_f32_e32 v17, v21, v17
	v_cvt_pk_bf16_f32 v18, v18, v19
	v_cvt_pk_bf16_f32 v19, v20, v17
	global_store_dwordx2 v[22:23], v[18:19], off
	s_waitcnt vmcnt(14)
	v_and_b32_e32 v52, 0xffff0000, v60
	v_lshlrev_b32_e32 v17, 16, v60
	v_mul_f32_e32 v59, v52, v52
	v_lshlrev_b32_e32 v53, 16, v61
	v_fmac_f32_e32 v59, v17, v17
	v_and_b32_e32 v54, 0xffff0000, v61
	v_fmac_f32_e32 v59, v53, v53
	v_lshlrev_b32_e32 v55, 16, v62
	v_fmac_f32_e32 v59, v54, v54
	v_and_b32_e32 v56, 0xffff0000, v62
	v_fmac_f32_e32 v59, v55, v55
	v_lshlrev_b32_e32 v57, 16, v63
	v_fmac_f32_e32 v59, v56, v56
	v_and_b32_e32 v58, 0xffff0000, v63
	s_waitcnt vmcnt(13)
	v_and_b32_e32 v60, 0xffff0000, v64
	v_lshlrev_b32_e32 v61, 16, v64
	v_fmac_f32_e32 v59, v57, v57
	v_pk_mul_f32 v[42:43], v[60:61], v[60:61]
	v_fmac_f32_e32 v59, v58, v58
	v_and_b32_e32 v62, 0xffff0000, v65
	v_lshlrev_b32_e32 v63, 16, v65
	v_add_f32_e32 v43, v43, v59
	v_pk_mul_f32 v[46:47], v[62:63], v[62:63]
	v_add_f32_e32 v42, v42, v43
	v_and_b32_e32 v64, 0xffff0000, v66
	v_lshlrev_b32_e32 v65, 16, v66
	v_add_f32_e32 v42, v47, v42
	v_pk_mul_f32 v[48:49], v[64:65], v[64:65]
	v_add_f32_e32 v42, v46, v42
	v_and_b32_e32 v66, 0xffff0000, v67
	v_lshlrev_b32_e32 v67, 16, v67
	v_add_f32_e32 v42, v49, v42
	v_pk_mul_f32 v[50:51], v[66:67], v[66:67]
	v_add_f32_e32 v42, v48, v42
	v_add_f32_e32 v42, v51, v42
	v_add_f32_e32 v42, v50, v42
	ds_bpermute_b32 v43, v16, v42
	s_waitcnt lgkmcnt(0)
	v_add_f32_e32 v42, v42, v43
	ds_bpermute_b32 v43, v15, v42
	s_waitcnt lgkmcnt(0)
	v_add_f32_e32 v42, v42, v43
	ds_bpermute_b32 v43, v14, v42
	s_waitcnt lgkmcnt(0)
	v_add_f32_e32 v42, v42, v43
	v_fmamk_f32 v42, v42, 0x3c000000, v3
	v_mul_f32_e32 v43, 0x4b800000, v42
	v_cmp_gt_f32_e32 vcc, s3, v42
	s_nop 1
	v_cndmask_b32_e32 v42, v42, v43, vcc
	v_rsq_f32_e32 v42, v42
	s_nop 0
	v_mul_f32_e32 v43, 0x45800000, v42
	v_cndmask_b32_e32 v42, v42, v43, vcc
	s_waitcnt vmcnt(12)
	v_mul_f32_e32 v68, v68, v42
	v_mul_f32_e32 v69, v69, v42
	v_mul_f32_e32 v70, v70, v42
	v_mul_f32_e32 v71, v71, v42
	s_waitcnt vmcnt(11)
	v_mul_f32_e32 v72, v72, v42
	v_mul_f32_e32 v73, v73, v42
	v_mul_f32_e32 v74, v74, v42
	v_mul_f32_e32 v75, v75, v42
	s_waitcnt vmcnt(10)
	v_mul_f32_e32 v76, v76, v42
	v_mul_f32_e32 v77, v77, v42
	v_mul_f32_e32 v78, v78, v42
	v_mul_f32_e32 v79, v79, v42
	s_waitcnt vmcnt(9)
	v_mul_f32_e32 v82, v82, v42
	v_mul_f32_e32 v80, v80, v42
	v_mul_f32_e32 v81, v81, v42
	v_mul_f32_e32 v83, v83, v42
	v_mul_f32_e32 v17, v68, v17
	v_mul_f32_e32 v68, v69, v52
	v_mul_f32_e32 v69, v70, v53
	v_mul_f32_e32 v70, v71, v54
	v_mul_f32_e32 v71, v72, v55
	v_mul_f32_e32 v72, v73, v56
	v_mul_f32_e32 v73, v74, v57
	v_mul_f32_e32 v74, v75, v58
	v_mul_f32_e32 v75, v76, v61
	v_mul_f32_e32 v76, v77, v60
	v_mul_f32_e32 v77, v78, v63
	v_mul_f32_e32 v78, v79, v62
	v_mul_f32_e32 v67, v82, v67
	v_cvt_pk_bf16_f32 v60, v17, v68
	v_cvt_pk_bf16_f32 v61, v69, v70
	v_cvt_pk_bf16_f32 v62, v71, v72
	v_cvt_pk_bf16_f32 v63, v73, v74
	v_mul_f32_e32 v79, v80, v65
	v_mul_f32_e32 v80, v81, v64
	v_mul_f32_e32 v81, v83, v66
	v_cvt_pk_bf16_f32 v64, v75, v76
	v_cvt_pk_bf16_f32 v65, v77, v78
	v_cvt_pk_bf16_f32 v66, v79, v80
	v_cvt_pk_bf16_f32 v67, v67, v81
	global_store_dwordx4 v[44:45], v[60:63], off
	global_store_dwordx4 v[44:45], v[64:67], off offset:16
	s_waitcnt vmcnt(9)
	v_lshlrev_b32_e32 v94, 16, v96
	v_and_b32_e32 v95, 0xffff0000, v96
	v_and_b32_e32 v96, 0xffff0000, v97
	v_lshlrev_b32_e32 v97, 16, v97
	v_pk_mul_f32 v[98:99], v[94:95], v[94:95]
	v_pk_mul_f32 v[100:101], v[96:97], v[96:97]
	v_add_f32_e32 v87, v98, v99
	v_add_f32_e32 v87, v101, v87
	v_add_f32_e32 v87, v100, v87
	ds_bpermute_b32 v98, v0, v87
	s_waitcnt lgkmcnt(0)
	v_add_f32_e32 v87, v87, v98
	ds_bpermute_b32 v98, v12, v87
	s_waitcnt lgkmcnt(0)
	v_add_f32_e32 v87, v87, v98
	ds_bpermute_b32 v98, v13, v87
	s_waitcnt lgkmcnt(0)
	v_add_f32_e32 v87, v87, v98
	ds_bpermute_b32 v98, v14, v87
	s_waitcnt lgkmcnt(0)
	v_add_f32_e32 v87, v87, v98
	ds_bpermute_b32 v98, v15, v87
	s_waitcnt lgkmcnt(0)
	v_add_f32_e32 v87, v87, v98
	ds_bpermute_b32 v98, v16, v87
	s_waitcnt lgkmcnt(0)
	v_add_f32_e32 v87, v87, v98
	v_fmamk_f32 v87, v87, 0x3b800000, v3
	v_mul_f32_e32 v98, 0x4b800000, v87
	v_cmp_gt_f32_e32 vcc, s3, v87
	s_nop 1
	v_cndmask_b32_e32 v87, v87, v98, vcc
	v_rsq_f32_e32 v87, v87
	s_nop 0
	v_mul_f32_e32 v98, 0x45800000, v87
	v_cndmask_b32_e32 v87, v87, v98, vcc
	v_mul_f32_e32 v94, v87, v94
	v_mul_f32_e32 v95, v87, v95
	v_mul_f32_e32 v97, v87, v97
	v_mul_f32_e32 v87, v87, v96
	v_mul_f32_e32 v88, v88, v94
	v_mul_f32_e32 v89, v89, v95
	v_mul_f32_e32 v90, v90, v97
	v_mul_f32_e32 v87, v91, v87
	v_cvt_pk_bf16_f32 v88, v88, v89
	v_cvt_pk_bf16_f32 v89, v90, v87
	global_store_dwordx2 v[92:93], v[88:89], off
	s_waitcnt vmcnt(9)
	v_and_b32_e32 v122, 0xffff0000, v160
	v_lshlrev_b32_e32 v87, 16, v160
	v_mul_f32_e32 v129, v122, v122
	v_lshlrev_b32_e32 v123, 16, v161
	v_fmac_f32_e32 v129, v87, v87
	v_and_b32_e32 v124, 0xffff0000, v161
	v_fmac_f32_e32 v129, v123, v123
	v_lshlrev_b32_e32 v125, 16, v162
	v_fmac_f32_e32 v129, v124, v124
	v_and_b32_e32 v126, 0xffff0000, v162
	v_fmac_f32_e32 v129, v125, v125
	v_lshlrev_b32_e32 v127, 16, v163
	v_fmac_f32_e32 v129, v126, v126
	v_and_b32_e32 v128, 0xffff0000, v163
	s_waitcnt vmcnt(8)
	v_and_b32_e32 v160, 0xffff0000, v164
	v_lshlrev_b32_e32 v161, 16, v164
	v_fmac_f32_e32 v129, v127, v127
	v_pk_mul_f32 v[112:113], v[160:161], v[160:161]
	v_fmac_f32_e32 v129, v128, v128
	v_and_b32_e32 v162, 0xffff0000, v165
	v_lshlrev_b32_e32 v163, 16, v165
	v_add_f32_e32 v113, v113, v129
	v_pk_mul_f32 v[116:117], v[162:163], v[162:163]
	v_add_f32_e32 v112, v112, v113
	v_and_b32_e32 v164, 0xffff0000, v166
	v_lshlrev_b32_e32 v165, 16, v166
	v_add_f32_e32 v112, v117, v112
	v_pk_mul_f32 v[118:119], v[164:165], v[164:165]
	v_add_f32_e32 v112, v116, v112
	v_and_b32_e32 v166, 0xffff0000, v167
	v_lshlrev_b32_e32 v167, 16, v167
	v_add_f32_e32 v112, v119, v112
	v_pk_mul_f32 v[120:121], v[166:167], v[166:167]
	v_add_f32_e32 v112, v118, v112
	v_add_f32_e32 v112, v121, v112
	v_add_f32_e32 v112, v120, v112
	ds_bpermute_b32 v113, v16, v112
	s_waitcnt lgkmcnt(0)
	v_add_f32_e32 v112, v112, v113
	ds_bpermute_b32 v113, v15, v112
	s_waitcnt lgkmcnt(0)
	v_add_f32_e32 v112, v112, v113
	ds_bpermute_b32 v113, v14, v112
	s_waitcnt lgkmcnt(0)
	v_add_f32_e32 v112, v112, v113
	v_fmamk_f32 v112, v112, 0x3c000000, v3
	v_mul_f32_e32 v113, 0x4b800000, v112
	v_cmp_gt_f32_e32 vcc, s3, v112
	s_nop 1
	v_cndmask_b32_e32 v112, v112, v113, vcc
	v_rsq_f32_e32 v112, v112
	s_nop 0
	v_mul_f32_e32 v113, 0x45800000, v112
	v_cndmask_b32_e32 v112, v112, v113, vcc
	s_waitcnt vmcnt(7)
	v_mul_f32_e32 v168, v168, v112
	v_mul_f32_e32 v169, v169, v112
	v_mul_f32_e32 v170, v170, v112
	v_mul_f32_e32 v171, v171, v112
	s_waitcnt vmcnt(6)
	v_mul_f32_e32 v172, v172, v112
	v_mul_f32_e32 v173, v173, v112
	v_mul_f32_e32 v174, v174, v112
	v_mul_f32_e32 v175, v175, v112
	s_waitcnt vmcnt(5)
	v_mul_f32_e32 v176, v176, v112
	v_mul_f32_e32 v177, v177, v112
	v_mul_f32_e32 v178, v178, v112
	v_mul_f32_e32 v179, v179, v112
	s_waitcnt vmcnt(4)
	v_mul_f32_e32 v182, v182, v112
	v_mul_f32_e32 v180, v180, v112
	v_mul_f32_e32 v181, v181, v112
	v_mul_f32_e32 v183, v183, v112
	v_mul_f32_e32 v87, v168, v87
	v_mul_f32_e32 v168, v169, v122
	v_mul_f32_e32 v169, v170, v123
	v_mul_f32_e32 v170, v171, v124
	v_mul_f32_e32 v171, v172, v125
	v_mul_f32_e32 v172, v173, v126
	v_mul_f32_e32 v173, v174, v127
	v_mul_f32_e32 v174, v175, v128
	v_mul_f32_e32 v175, v176, v161
	v_mul_f32_e32 v176, v177, v160
	v_mul_f32_e32 v177, v178, v163
	v_mul_f32_e32 v178, v179, v162
	v_mul_f32_e32 v167, v182, v167
	v_cvt_pk_bf16_f32 v160, v87, v168
	v_cvt_pk_bf16_f32 v161, v169, v170
	v_cvt_pk_bf16_f32 v162, v171, v172
	v_cvt_pk_bf16_f32 v163, v173, v174
	v_mul_f32_e32 v179, v180, v165
	v_mul_f32_e32 v180, v181, v164
	v_mul_f32_e32 v181, v183, v166
	v_cvt_pk_bf16_f32 v164, v175, v176
	v_cvt_pk_bf16_f32 v165, v177, v178
	v_cvt_pk_bf16_f32 v166, v179, v180
	v_cvt_pk_bf16_f32 v167, v167, v181
	global_store_dwordx4 v[114:115], v[160:163], off
	global_store_dwordx4 v[114:115], v[164:167], off offset:16
	s_andn2_b64 exec, exec, s[14:15]
	s_cbranch_execnz .Lp3_fast
	s_branch .LBB0_556
.LBB0_555:
	v_lshl_add_u64 v[22:23], s[76:77], 0, v[10:11]
	v_add_co_u32_e32 v26, vcc, 0x1e738000, v22
	global_load_dwordx4 v[18:21], v[4:5], off
	s_nop 0
	v_addc_co_u32_e32 v27, vcc, 0, v23, vcc
	global_load_dwordx2 v[26:27], v[26:27], off
	v_add_co_u32_e64 v22, s[4:5], s9, v22
	v_lshl_add_u64 v[24:25], s[76:77], 0, v[8:9]
	s_nop 0
	v_addc_co_u32_e64 v23, vcc, 0, v23, s[4:5]
	v_add_co_u32_e32 v44, vcc, s18, v24
	v_lshl_add_u64 v[42:43], v[24:25], 0, s[16:17]
	s_nop 0
	v_addc_co_u32_e32 v45, vcc, 0, v25, vcc
	v_add_u32_e32 v2, s8, v2
	v_cmp_lt_i32_e32 vcc, s19, v2
	s_or_b64 s[14:15], vcc, s[14:15]
	v_lshl_add_u64 v[8:9], v[8:9], 0, s[10:11]
	v_lshl_add_u64 v[10:11], v[10:11], 0, s[12:13]
	global_load_dwordx4 v[60:63], v[44:45], off
	global_load_dwordx4 v[64:67], v[42:43], off offset:16
	global_load_dwordx4 v[68:71], v[6:7], off
	global_load_dwordx4 v[72:75], v[6:7], off offset:16
	global_load_dwordx4 v[76:79], v[6:7], off offset:32
	global_load_dwordx4 v[80:83], v[6:7], off offset:48
	s_waitcnt vmcnt(6)
	v_lshlrev_b32_e32 v24, 16, v26
	v_and_b32_e32 v25, 0xffff0000, v26
	v_and_b32_e32 v26, 0xffff0000, v27
	v_lshlrev_b32_e32 v27, 16, v27
	v_pk_mul_f32 v[28:29], v[24:25], v[24:25]
	v_pk_mul_f32 v[30:31], v[26:27], v[26:27]
	v_add_f32_e32 v17, v28, v29
	v_add_f32_e32 v17, v31, v17
	v_add_f32_e32 v17, v30, v17
	ds_bpermute_b32 v28, v0, v17
	s_waitcnt lgkmcnt(0)
	v_add_f32_e32 v17, v17, v28
	ds_bpermute_b32 v28, v12, v17
	s_waitcnt lgkmcnt(0)
	v_add_f32_e32 v17, v17, v28
	ds_bpermute_b32 v28, v13, v17
	s_waitcnt lgkmcnt(0)
	v_add_f32_e32 v17, v17, v28
	ds_bpermute_b32 v28, v14, v17
	s_waitcnt lgkmcnt(0)
	v_add_f32_e32 v17, v17, v28
	ds_bpermute_b32 v28, v15, v17
	s_waitcnt lgkmcnt(0)
	v_add_f32_e32 v17, v17, v28
	ds_bpermute_b32 v28, v16, v17
	s_waitcnt lgkmcnt(0)
	v_add_f32_e32 v17, v17, v28
	v_fmamk_f32 v17, v17, 0x3b800000, v3
	v_mul_f32_e32 v28, 0x4b800000, v17
	v_cmp_gt_f32_e32 vcc, s3, v17
	s_nop 1
	v_cndmask_b32_e32 v17, v17, v28, vcc
	v_rsq_f32_e32 v17, v17
	s_nop 0
	v_mul_f32_e32 v28, 0x45800000, v17
	v_cndmask_b32_e32 v17, v17, v28, vcc
	v_mul_f32_e32 v24, v17, v24
	v_mul_f32_e32 v25, v17, v25
	v_mul_f32_e32 v27, v17, v27
	v_mul_f32_e32 v17, v17, v26
	v_mul_f32_e32 v18, v18, v24
	v_mul_f32_e32 v19, v19, v25
	v_mul_f32_e32 v20, v20, v27
	v_mul_f32_e32 v17, v21, v17
	v_cvt_pk_bf16_f32 v18, v18, v19
	v_cvt_pk_bf16_f32 v19, v20, v17
	global_store_dwordx2 v[22:23], v[18:19], off
	s_waitcnt vmcnt(6)
	v_and_b32_e32 v52, 0xffff0000, v60
	v_lshlrev_b32_e32 v17, 16, v60
	v_mul_f32_e32 v59, v52, v52
	v_lshlrev_b32_e32 v53, 16, v61
	v_fmac_f32_e32 v59, v17, v17
	v_and_b32_e32 v54, 0xffff0000, v61
	v_fmac_f32_e32 v59, v53, v53
	v_lshlrev_b32_e32 v55, 16, v62
	v_fmac_f32_e32 v59, v54, v54
	v_and_b32_e32 v56, 0xffff0000, v62
	v_fmac_f32_e32 v59, v55, v55
	v_lshlrev_b32_e32 v57, 16, v63
	v_fmac_f32_e32 v59, v56, v56
	v_and_b32_e32 v58, 0xffff0000, v63
	s_waitcnt vmcnt(5)
	v_and_b32_e32 v60, 0xffff0000, v64
	v_lshlrev_b32_e32 v61, 16, v64
	v_fmac_f32_e32 v59, v57, v57
	v_pk_mul_f32 v[42:43], v[60:61], v[60:61]
	v_fmac_f32_e32 v59, v58, v58
	v_and_b32_e32 v62, 0xffff0000, v65
	v_lshlrev_b32_e32 v63, 16, v65
	v_add_f32_e32 v43, v43, v59
	v_pk_mul_f32 v[46:47], v[62:63], v[62:63]
	v_add_f32_e32 v42, v42, v43
	v_and_b32_e32 v64, 0xffff0000, v66
	v_lshlrev_b32_e32 v65, 16, v66
	v_add_f32_e32 v42, v47, v42
	v_pk_mul_f32 v[48:49], v[64:65], v[64:65]
	v_add_f32_e32 v42, v46, v42
	v_and_b32_e32 v66, 0xffff0000, v67
	v_lshlrev_b32_e32 v67, 16, v67
	v_add_f32_e32 v42, v49, v42
	v_pk_mul_f32 v[50:51], v[66:67], v[66:67]
	v_add_f32_e32 v42, v48, v42
	v_add_f32_e32 v42, v51, v42
	v_add_f32_e32 v42, v50, v42
	ds_bpermute_b32 v43, v16, v42
	s_waitcnt lgkmcnt(0)
	v_add_f32_e32 v42, v42, v43
	ds_bpermute_b32 v43, v15, v42
	s_waitcnt lgkmcnt(0)
	v_add_f32_e32 v42, v42, v43
	ds_bpermute_b32 v43, v14, v42
	s_waitcnt lgkmcnt(0)
	v_add_f32_e32 v42, v42, v43
	v_fmamk_f32 v42, v42, 0x3c000000, v3
	v_mul_f32_e32 v43, 0x4b800000, v42
	v_cmp_gt_f32_e32 vcc, s3, v42
	s_nop 1
	v_cndmask_b32_e32 v42, v42, v43, vcc
	v_rsq_f32_e32 v42, v42
	s_nop 0
	v_mul_f32_e32 v43, 0x45800000, v42
	v_cndmask_b32_e32 v42, v42, v43, vcc
	s_waitcnt vmcnt(4)
	v_mul_f32_e32 v68, v68, v42
	v_mul_f32_e32 v69, v69, v42
	v_mul_f32_e32 v70, v70, v42
	v_mul_f32_e32 v71, v71, v42
	s_waitcnt vmcnt(3)
	v_mul_f32_e32 v72, v72, v42
	v_mul_f32_e32 v73, v73, v42
	v_mul_f32_e32 v74, v74, v42
	v_mul_f32_e32 v75, v75, v42
	s_waitcnt vmcnt(2)
	v_mul_f32_e32 v76, v76, v42
	v_mul_f32_e32 v77, v77, v42
	v_mul_f32_e32 v78, v78, v42
	v_mul_f32_e32 v79, v79, v42
	s_waitcnt vmcnt(1)
	v_mul_f32_e32 v82, v82, v42
	v_mul_f32_e32 v80, v80, v42
	v_mul_f32_e32 v81, v81, v42
	v_mul_f32_e32 v83, v83, v42
	v_mul_f32_e32 v17, v68, v17
	v_mul_f32_e32 v68, v69, v52
	v_mul_f32_e32 v69, v70, v53
	v_mul_f32_e32 v70, v71, v54
	v_mul_f32_e32 v71, v72, v55
	v_mul_f32_e32 v72, v73, v56
	v_mul_f32_e32 v73, v74, v57
	v_mul_f32_e32 v74, v75, v58
	v_mul_f32_e32 v75, v76, v61
	v_mul_f32_e32 v76, v77, v60
	v_mul_f32_e32 v77, v78, v63
	v_mul_f32_e32 v78, v79, v62
	v_mul_f32_e32 v67, v82, v67
	v_cvt_pk_bf16_f32 v60, v17, v68
	v_cvt_pk_bf16_f32 v61, v69, v70
	v_cvt_pk_bf16_f32 v62, v71, v72
	v_cvt_pk_bf16_f32 v63, v73, v74
	v_mul_f32_e32 v79, v80, v65
	v_mul_f32_e32 v80, v81, v64
	v_mul_f32_e32 v81, v83, v66
	v_cvt_pk_bf16_f32 v64, v75, v76
	v_cvt_pk_bf16_f32 v65, v77, v78
	v_cvt_pk_bf16_f32 v66, v79, v80
	v_cvt_pk_bf16_f32 v67, v67, v81
	global_store_dwordx4 v[44:45], v[60:63], off
	global_store_dwordx4 v[44:45], v[64:67], off offset:16
	s_andn2_b64 exec, exec, s[14:15]
	s_cbranch_execnz .LBB0_555
